# p_prep token loop: loads of all four conv taps issued up front for tokens t>=3 (one memory round trip per token instead of four; arithmetic unchanged), on top of the batched p_mpost loop
# baseline (speedup 1.0000x reference)
.LBB0_411:
	v_readlane_b32 s0, v254, 49
	s_add_i32 s0, s0, s2
	s_ashr_i32 s1, s0, 31
	s_lshr_b32 s3, s1, 21
	s_add_i32 s3, s0, s3
	s_and_b32 s3, s3, 0xfffff800
	s_sub_i32 s3, s0, s3
	s_cmp_lt_i32 s3, 3
	v_lshlrev_b32_e32 v0, 1, v2
	s_cbranch_scc1 .Lprep_slow
	s_add_i32 s4, s0, -3
	s_mul_hi_i32 s5, s4, 0x5000
	s_mulk_i32 s4, 0x5000
	v_readlane_b32 s6, v255, 0
	v_readlane_b32 s7, v255, 1
	s_add_u32 s4, s6, s4
	s_addc_u32 s5, s7, s5
	s_add_u32 s4, s4, 0x33501680
	s_addc_u32 s5, s5, 0
	s_add_u32 s56, s4, 0x5000
	s_addc_u32 s57, s5, 0
	s_add_u32 s58, s4, 0xa000
	s_addc_u32 s59, s5, 0
	s_add_u32 s60, s4, 0xf000
	s_addc_u32 s61, s5, 0
	global_load_dwordx4 v[138:141], v0, s[4:5]
	global_load_dwordx4 v[142:145], v0, s[4:5] offset:16
	global_load_dwordx4 v[146:149], v0, s[56:57]
	global_load_dwordx4 v[150:153], v0, s[56:57] offset:16
	global_load_dwordx4 v[154:157], v0, s[58:59]
	global_load_dwordx4 v[158:161], v0, s[58:59] offset:16
	global_load_dwordx4 v[162:165], v0, s[60:61]
	global_load_dwordx4 v[166:169], v0, s[60:61] offset:16
	s_waitcnt vmcnt(7)
	v_lshlrev_b32_e32 v170, 16, v138
	v_and_b32_e32 v171, 0xffff0000, v138
	v_lshlrev_b32_e32 v172, 16, v139
	v_and_b32_e32 v173, 0xffff0000, v139
	v_lshlrev_b32_e32 v174, 16, v140
	v_and_b32_e32 v175, 0xffff0000, v140
	v_lshlrev_b32_e32 v176, 16, v141
	v_and_b32_e32 v177, 0xffff0000, v141
	v_pk_fma_f32 v[106:107], v[18:19], v[170:171], v[82:83]
	v_pk_fma_f32 v[104:105], v[20:21], v[172:173], v[84:85]
	v_pk_fma_f32 v[102:103], v[14:15], v[174:175], v[78:79]
	v_pk_fma_f32 v[100:101], v[16:17], v[176:177], v[80:81]
	s_waitcnt vmcnt(6)
	v_lshlrev_b32_e32 v178, 16, v142
	v_and_b32_e32 v179, 0xffff0000, v142
	v_lshlrev_b32_e32 v180, 16, v143
	v_and_b32_e32 v181, 0xffff0000, v143
	v_lshlrev_b32_e32 v182, 16, v144
	v_and_b32_e32 v183, 0xffff0000, v144
	v_lshlrev_b32_e32 v184, 16, v145
	v_and_b32_e32 v185, 0xffff0000, v145
	v_pk_fma_f32 v[98:99], v[10:11], v[178:179], v[74:75]
	v_pk_fma_f32 v[96:97], v[12:13], v[180:181], v[76:77]
	v_pk_fma_f32 v[94:95], v[6:7], v[182:183], v[70:71]
	v_pk_fma_f32 v[92:93], v[8:9], v[184:185], v[72:73]
	s_waitcnt vmcnt(5)
	v_lshlrev_b32_e32 v170, 16, v146
	v_and_b32_e32 v171, 0xffff0000, v146
	v_lshlrev_b32_e32 v172, 16, v147
	v_and_b32_e32 v173, 0xffff0000, v147
	v_lshlrev_b32_e32 v174, 16, v148
	v_and_b32_e32 v175, 0xffff0000, v148
	v_lshlrev_b32_e32 v176, 16, v149
	v_and_b32_e32 v177, 0xffff0000, v149
	v_pk_fma_f32 v[106:107], v[30:31], v[170:171], v[106:107]
	v_pk_fma_f32 v[104:105], v[32:33], v[172:173], v[104:105]
	v_pk_fma_f32 v[102:103], v[26:27], v[174:175], v[102:103]
	v_pk_fma_f32 v[100:101], v[28:29], v[176:177], v[100:101]
	s_waitcnt vmcnt(4)
	v_lshlrev_b32_e32 v178, 16, v150
	v_and_b32_e32 v179, 0xffff0000, v150
	v_lshlrev_b32_e32 v180, 16, v151
	v_and_b32_e32 v181, 0xffff0000, v151
	v_lshlrev_b32_e32 v182, 16, v152
	v_and_b32_e32 v183, 0xffff0000, v152
	v_lshlrev_b32_e32 v184, 16, v153
	v_and_b32_e32 v185, 0xffff0000, v153
	v_pk_fma_f32 v[98:99], v[22:23], v[178:179], v[98:99]
	v_pk_fma_f32 v[96:97], v[24:25], v[180:181], v[96:97]
	v_pk_fma_f32 v[94:95], v[46:47], v[182:183], v[94:95]
	v_pk_fma_f32 v[92:93], v[48:49], v[184:185], v[92:93]
	s_waitcnt vmcnt(3)
	v_lshlrev_b32_e32 v170, 16, v154
	v_and_b32_e32 v171, 0xffff0000, v154
	v_lshlrev_b32_e32 v172, 16, v155
	v_and_b32_e32 v173, 0xffff0000, v155
	v_lshlrev_b32_e32 v174, 16, v156
	v_and_b32_e32 v175, 0xffff0000, v156
	v_lshlrev_b32_e32 v176, 16, v157
	v_and_b32_e32 v177, 0xffff0000, v157
	v_pk_fma_f32 v[106:107], v[34:35], v[170:171], v[106:107]
	v_pk_fma_f32 v[104:105], v[36:37], v[172:173], v[104:105]
	v_pk_fma_f32 v[102:103], v[50:51], v[174:175], v[102:103]
	v_pk_fma_f32 v[100:101], v[52:53], v[176:177], v[100:101]
	s_waitcnt vmcnt(2)
	v_lshlrev_b32_e32 v178, 16, v158
	v_and_b32_e32 v179, 0xffff0000, v158
	v_lshlrev_b32_e32 v180, 16, v159
	v_and_b32_e32 v181, 0xffff0000, v159
	v_lshlrev_b32_e32 v182, 16, v160
	v_and_b32_e32 v183, 0xffff0000, v160
	v_lshlrev_b32_e32 v184, 16, v161
	v_and_b32_e32 v185, 0xffff0000, v161
	v_pk_fma_f32 v[98:99], v[42:43], v[178:179], v[98:99]
	v_pk_fma_f32 v[96:97], v[44:45], v[180:181], v[96:97]
	v_pk_fma_f32 v[94:95], v[38:39], v[182:183], v[94:95]
	v_pk_fma_f32 v[92:93], v[40:41], v[184:185], v[92:93]
	s_waitcnt vmcnt(1)
	v_lshlrev_b32_e32 v170, 16, v162
	v_and_b32_e32 v171, 0xffff0000, v162
	v_lshlrev_b32_e32 v172, 16, v163
	v_and_b32_e32 v173, 0xffff0000, v163
	v_lshlrev_b32_e32 v174, 16, v164
	v_and_b32_e32 v175, 0xffff0000, v164
	v_lshlrev_b32_e32 v176, 16, v165
	v_and_b32_e32 v177, 0xffff0000, v165
	v_pk_fma_f32 v[106:107], v[54:55], v[170:171], v[106:107]
	v_pk_fma_f32 v[104:105], v[56:57], v[172:173], v[104:105]
	v_pk_fma_f32 v[102:103], v[66:67], v[174:175], v[102:103]
	v_pk_fma_f32 v[100:101], v[68:69], v[176:177], v[100:101]
	s_waitcnt vmcnt(0)
	v_lshlrev_b32_e32 v178, 16, v166
	v_and_b32_e32 v179, 0xffff0000, v166
	v_lshlrev_b32_e32 v180, 16, v167
	v_and_b32_e32 v181, 0xffff0000, v167
	v_lshlrev_b32_e32 v182, 16, v168
	v_and_b32_e32 v183, 0xffff0000, v168
	v_lshlrev_b32_e32 v184, 16, v169
	v_and_b32_e32 v185, 0xffff0000, v169
	v_pk_fma_f32 v[98:99], v[62:63], v[178:179], v[98:99]
	v_pk_fma_f32 v[96:97], v[64:65], v[180:181], v[96:97]
	v_pk_fma_f32 v[94:95], v[58:59], v[182:183], v[94:95]
	v_pk_fma_f32 v[92:93], v[60:61], v[184:185], v[92:93]
	s_branch .LBB0_410
.Lprep_slow:
	s_waitcnt vmcnt(0)
	v_mov_b32_e32 v106, v82
	v_mov_b32_e32 v107, v83
	v_mov_b32_e32 v104, v84
	v_mov_b32_e32 v105, v85
	v_mov_b32_e32 v102, v78
	v_mov_b32_e32 v103, v79
	v_mov_b32_e32 v100, v80
	v_mov_b32_e32 v101, v81
	v_mov_b32_e32 v98, v74
	v_mov_b32_e32 v99, v75
	v_mov_b32_e32 v96, v76
	v_mov_b32_e32 v97, v77
	v_mov_b32_e32 v94, v70
	v_mov_b32_e32 v95, v71
	v_mov_b32_e32 v92, v72
	v_mov_b32_e32 v93, v73
	s_branch .LBB0_417
